# in_proj unit order: column tiles permuted so each workgroup gets a mix of sigmoid-gate and plain epilogues (was all-sigmoid on odd XCDs)
# speedup vs baseline: 1.0050x; 1.0039x over previous
.LBB0_167:
	s_or_b64 exec, exec, s[38:39]
	v_mov_b32_e32 v145, v144
	v_readlane_b32 s0, v247, 7
	s_waitcnt lgkmcnt(0)
	s_barrier
	v_readlane_b32 s16, v247, 9
	v_add_u32_e32 v0, s0, v145
	s_cmpk_lt_i32 s2, 0x5e0
	v_readlane_b32 s17, v247, 10
	s_cselect_b64 s[4:5], -1, 0
	s_cmpk_gt_i32 s2, 0x5df
	v_readfirstlane_b32 s10, v0
	s_cbranch_scc1 .LBB0_169
	s_ashr_i32 s0, s2, 31
	s_lshr_b32 s0, s0, 29
	s_add_i32 s0, s2, s0
	s_ashr_i32 s1, s0, 3
	s_and_b32 s0, s0, -8
	s_sub_i32 s0, s2, s0
	s_cmp_lt_i32 s0, 0
	s_movk_i32 s6, 0xbd
	s_cselect_b32 s6, s6, 0xbc
	s_mul_i32 s0, s6, s0
	s_add_i32 s0, s0, s1
	s_mul_hi_i32 s1, s0, 0xae4c415d
	s_add_i32 s1, s1, s0
	s_lshr_b32 s6, s1, 31
	s_ashr_i32 s1, s1, 8
	s_add_i32 s1, s1, s6
	s_lshl_b32 s6, s1, 3
	s_mulk_i32 s1, 0x178
	s_sub_i32 s0, s0, s1
	s_sext_i32_i16 s1, s0
	s_bfe_u32 s1, s1, 0x3001c
	s_add_i32 s1, s0, s1
	s_sext_i32_i16 s7, s1
	s_and_b32 s1, s1, 0xfff8
	s_sub_i32 s0, s0, s1
	s_sext_i32_i16 s0, s0
	s_add_i32 s62, s6, s0
	s_ashr_i32 s6, s7, 3
	s_lshr_b32 s0, s6, 3
	s_and_b32 s1, s6, 3
	s_lshl2_add_u32 s0, s0, s1
	s_add_i32 s1, s0, 22
	s_cmp_eq_u32 s0, 22
	s_cselect_b32 s0, 46, s0
	s_bitcmp1_b32 s6, 2
	s_cselect_b32 s6, s0, s1

.LBB0_175:
	s_add_i32 s57, s57, 1
	s_mul_i32 s4, s57, s63
	s_mul_hi_u32 s5, s57, s3
	s_add_i32 s5, s5, s4
	s_mul_i32 s4, s57, s3
	s_add_u32 s10, s4, s2
	s_addc_u32 s11, s5, s64
	v_cmp_gt_i64_e32 vcc, s[10:11], v[148:149]
	v_cmp_lt_i64_e64 s[4:5], s[10:11], v[146:147]
	s_cbranch_vccnz .LBB0_177
	s_ashr_i32 s7, s10, 31
	s_lshr_b32 s7, s7, 29
	s_add_i32 s7, s10, s7
	s_ashr_i32 s11, s7, 3
	s_and_b32 s7, s7, -8
	s_sub_i32 s7, s10, s7
	s_cmp_lt_i32 s7, 0
	s_cselect_b32 s10, s65, 0xbc
	s_mul_i32 s7, s10, s7
	s_add_i32 s7, s7, s11
	s_mul_hi_i32 s10, s7, 0xae4c415d
	s_add_i32 s10, s10, s7
	s_lshr_b32 s11, s10, 31
	s_ashr_i32 s10, s10, 8
	s_add_i32 s10, s10, s11
	s_lshl_b32 s11, s10, 3
	s_sub_i32 s46, 32, s11
	s_min_i32 s47, s46, 8
	s_abs_i32 s46, s47
	v_cvt_f32_u32_e32 v0, s46
	s_sub_i32 s49, 0, s46
	s_mulk_i32 s10, 0x178
	s_sub_i32 s7, s7, s10
	v_rcp_iflag_f32_e32 v0, v0
	s_abs_i32 s10, s7
	s_xor_b32 s48, s7, s47
	s_ashr_i32 s48, s48, 31
	v_mul_f32_e32 v0, 0x4f7ffffe, v0
	v_cvt_u32_f32_e32 v0, v0
	s_nop 0
	v_readfirstlane_b32 s52, v0
	s_mul_i32 s49, s49, s52
	s_mul_hi_u32 s49, s52, s49
	s_add_i32 s52, s52, s49
	s_mul_hi_u32 s49, s10, s52
	s_mul_i32 s52, s49, s46
	s_sub_i32 s10, s10, s52
	s_add_i32 s53, s49, 1
	s_sub_i32 s52, s10, s46
	s_cmp_ge_u32 s10, s46
	s_cselect_b32 s49, s53, s49
	s_cselect_b32 s10, s52, s10
	s_add_i32 s52, s49, 1
	s_cmp_ge_u32 s10, s46
	s_cselect_b32 s10, s52, s49
	s_xor_b32 s10, s10, s48
	s_sub_i32 s46, s10, s48
	s_mul_i32 s10, s46, s47
	s_sub_i32 s7, s7, s10
	s_add_i32 s69, s7, s11
	s_lshr_b32 s10, s46, 3
	s_and_b32 s11, s46, 3
	s_lshl2_add_u32 s10, s10, s11
	s_add_i32 s11, s10, 22
	s_cmp_eq_u32 s10, 22
	s_cselect_b32 s10, 46, s10
	s_bitcmp1_b32 s46, 2
	s_cselect_b32 s46, s10, s11

.LBB0_1558:
	s_or_b64 exec, exec, s[42:43]
	v_mov_b32_e32 v145, v144
	v_readlane_b32 s0, v247, 7
	s_waitcnt lgkmcnt(0)
	s_barrier
	v_readlane_b32 s14, v247, 9
	v_add_u32_e32 v0, s0, v145
	v_readlane_b32 s0, v247, 21
	v_readlane_b32 s1, v247, 22
	v_readlane_b32 s15, v247, 10
	s_and_b64 vcc, exec, s[0:1]
	v_readfirstlane_b32 s10, v0
	s_cbranch_vccnz .LBB0_1560
	s_ashr_i32 s0, s2, 31
	s_lshr_b32 s0, s0, 29
	s_add_i32 s0, s2, s0
	s_ashr_i32 s1, s0, 3
	s_and_b32 s0, s0, -8
	s_sub_i32 s0, s2, s0
	s_cmp_lt_i32 s0, 0
	s_movk_i32 s4, 0xbd
	s_cselect_b32 s4, s4, 0xbc
	s_mul_i32 s0, s4, s0
	s_add_i32 s0, s0, s1
	s_mul_hi_i32 s1, s0, 0xae4c415d
	s_add_i32 s1, s1, s0
	s_lshr_b32 s4, s1, 31
	s_ashr_i32 s1, s1, 8
	s_add_i32 s1, s1, s4
	s_lshl_b32 s4, s1, 3
	s_mulk_i32 s1, 0x178
	s_sub_i32 s0, s0, s1
	s_sext_i32_i16 s1, s0
	s_bfe_u32 s1, s1, 0x3001c
	s_add_i32 s1, s0, s1
	s_sext_i32_i16 s5, s1
	s_and_b32 s1, s1, 0xfff8
	s_sub_i32 s0, s0, s1
	s_sext_i32_i16 s0, s0
	s_add_i32 s61, s4, s0
	s_ashr_i32 s12, s5, 3
	s_lshr_b32 s0, s12, 3
	s_and_b32 s1, s12, 3
	s_lshl2_add_u32 s0, s0, s1
	s_add_i32 s1, s0, 22
	s_cmp_eq_u32 s0, 22
	s_cselect_b32 s0, 46, s0
	s_bitcmp1_b32 s12, 2
	s_cselect_b32 s12, s0, s1

.LBB0_1566:
	s_add_i32 s48, s48, 1
	s_mul_i32 s8, s48, s52
	s_mul_hi_u32 s9, s48, s3
	s_add_i32 s9, s9, s8
	s_mul_i32 s8, s48, s3
	s_add_u32 s8, s8, s2
	s_addc_u32 s9, s9, s53
	v_cmp_gt_i64_e32 vcc, s[8:9], v[148:149]
	v_cmp_lt_i64_e64 s[10:11], s[8:9], v[146:147]
	s_cbranch_vccnz .LBB0_1568
	s_ashr_i32 s9, s8, 31
	s_lshr_b32 s9, s9, 29
	s_add_i32 s9, s8, s9
	s_ashr_i32 s13, s9, 3
	s_and_b32 s9, s9, -8
	s_sub_i32 s8, s8, s9
	s_cmp_lt_i32 s8, 0
	s_movk_i32 s9, 0xbd
	s_cselect_b32 s9, s9, 0xbc
	s_mul_i32 s8, s9, s8
	s_add_i32 s8, s8, s13
	s_mul_hi_i32 s9, s8, 0xae4c415d
	s_add_i32 s9, s9, s8
	s_lshr_b32 s13, s9, 31
	s_ashr_i32 s9, s9, 8
	s_add_i32 s9, s9, s13
	s_lshl_b32 s13, s9, 3
	s_sub_i32 s38, 32, s13
	s_min_i32 s39, s38, 8
	s_abs_i32 s38, s39
	v_cvt_f32_u32_e32 v0, s38
	s_sub_i32 s41, 0, s38
	s_mulk_i32 s9, 0x178
	s_sub_i32 s8, s8, s9
	v_rcp_iflag_f32_e32 v0, v0
	s_abs_i32 s9, s8
	s_xor_b32 s40, s8, s39
	s_ashr_i32 s40, s40, 31
	v_mul_f32_e32 v0, 0x4f7ffffe, v0
	v_cvt_u32_f32_e32 v0, v0
	s_nop 0
	v_readfirstlane_b32 s44, v0
	s_mul_i32 s41, s41, s44
	s_mul_hi_u32 s41, s44, s41
	s_add_i32 s44, s44, s41
	s_mul_hi_u32 s41, s9, s44
	s_mul_i32 s44, s41, s38
	s_sub_i32 s9, s9, s44
	s_add_i32 s45, s41, 1
	s_sub_i32 s44, s9, s38
	s_cmp_ge_u32 s9, s38
	s_cselect_b32 s41, s45, s41
	s_cselect_b32 s9, s44, s9
	s_add_i32 s44, s41, 1
	s_cmp_ge_u32 s9, s38
	s_cselect_b32 s9, s44, s41
	s_xor_b32 s9, s9, s40
	s_sub_i32 s38, s9, s40
	s_mul_i32 s9, s38, s39
	s_sub_i32 s8, s8, s9
	s_add_i32 s60, s8, s13
	s_lshr_b32 s8, s38, 3
	s_and_b32 s9, s38, 3
	s_lshl2_add_u32 s8, s8, s9
	s_add_i32 s9, s8, 22
	s_cmp_eq_u32 s8, 22
	s_cselect_b32 s8, 46, s8
	s_bitcmp1_b32 s38, 2
	s_cselect_b32 s38, s8, s9
